# agg1: 8-row ring buffer (two stage buffers, per-row re-issue, vmcnt(7)), MFMA acc moved from AGPR to VGPR; no gain: agg1 is memory-throughput-bound
# speedup vs baseline: 1.0057x; 1.0057x over previous
.LBB3_4:
	s_waitcnt vmcnt(4)
	v_lshlrev_b32_sdwa v0, v78, v70 dst_sel:DWORD dst_unused:UNUSED_PAD src0_sel:DWORD src1_sel:WORD_0
	s_waitcnt vmcnt(3) lgkmcnt(1)
	v_lshlrev_b32_sdwa v10, v78, v72 dst_sel:DWORD dst_unused:UNUSED_PAD src0_sel:DWORD src1_sel:WORD_0
	s_waitcnt vmcnt(2)
	v_lshlrev_b32_sdwa v11, v78, v71 dst_sel:DWORD dst_unused:UNUSED_PAD src0_sel:DWORD src1_sel:WORD_0
	s_waitcnt vmcnt(1) lgkmcnt(0)
	v_lshlrev_b32_sdwa v12, v78, v73 dst_sel:DWORD dst_unused:UNUSED_PAD src0_sel:DWORD src1_sel:WORD_0
	global_load_dwordx2 v[48:49], v0, s[22:23]
	global_load_dwordx2 v[46:47], v10, s[22:23]
	global_load_dwordx2 v[44:45], v11, s[22:23]
	global_load_dwordx2 v[28:29], v12, s[22:23]
	v_lshlrev_b32_sdwa v0, v79, v70 dst_sel:DWORD dst_unused:UNUSED_PAD src0_sel:DWORD src1_sel:WORD_0
	v_lshlrev_b32_sdwa v10, v79, v72 dst_sel:DWORD dst_unused:UNUSED_PAD src0_sel:DWORD src1_sel:WORD_0
	ds_write2_b32 v66, v0, v10 offset1:16
	v_lshlrev_b32_sdwa v0, v79, v71 dst_sel:DWORD dst_unused:UNUSED_PAD src0_sel:DWORD src1_sel:WORD_0
	v_lshlrev_b32_sdwa v10, v79, v73 dst_sel:DWORD dst_unused:UNUSED_PAD src0_sel:DWORD src1_sel:WORD_0
	ds_write2_b32 v66, v0, v10 offset0:32 offset1:48
	ds_read_b128 v[16:19], v64
	ds_read_b128 v[98:101], v64 offset:16
	v_add_u32_e32 v10, s44, v33
	v_mov_b32_e32 v0, v62
	v_min_i32_e32 v62, 0x30d3, v10
	v_mov_b64_e32 v[40:41], v[94:95]
	s_waitcnt lgkmcnt(0)
	v_add_u32_e32 v20, v17, v31
	v_add_u32_e32 v21, v16, v30
	v_add_u32_e32 v50, v19, v31
	v_add_u32_e32 v51, v18, v30
	global_load_dwordx4 v[10:13], v21, s[20:21]
	global_load_dwordx4 v[14:17], v20, s[20:21]
	s_nop 0
	global_load_dwordx4 v[18:21], v51, s[20:21]
	global_load_dwordx4 v[22:25], v50, s[20:21]
	v_add_u32_e32 v98, v98, v30
	v_add_u32_e32 v99, v99, v30
	v_add_u32_e32 v100, v100, v30
	v_add_u32_e32 v101, v101, v30
	global_load_dwordx4 v[110:113], v98, s[20:21]
	global_load_dwordx4 v[114:117], v99, s[20:21]
	global_load_dwordx4 v[118:121], v100, s[20:21]
	global_load_dwordx4 v[122:125], v101, s[20:21]
	v_lshl_or_b32 v50, v62, 2, v35
	v_ashrrev_i32_e32 v51, 31, v50
	v_lshl_add_u64 v[50:51], v[50:51], 2, s[16:17]
	global_load_dwordx2 v[94:95], v[50:51], off
	v_add_u32_e32 v50, -1, v41
	v_add_u32_e32 v51, v40, v58
	v_add_u32_e32 v52, v59, v40
	v_add_u32_e32 v53, v60, v40
	v_add_u32_e32 v54, v61, v40
	v_min_i32_e32 v51, v51, v50
	v_min_i32_e32 v52, v52, v50
	v_min_i32_e32 v53, v53, v50
	v_min_i32_e32 v50, v54, v50
	v_max_i32_e32 v51, 0, v51
	v_max_i32_e32 v50, 0, v50
	v_lshlrev_b32_e32 v51, 1, v51
	v_max_i32_e32 v52, 0, v52
	v_max_i32_e32 v53, 0, v53
	v_lshlrev_b32_e32 v50, 1, v50
	v_lshlrev_b32_e32 v52, 1, v52
	v_lshlrev_b32_e32 v53, 1, v53
	global_load_ushort v70, v51, s[18:19]
	global_load_ushort v72, v52, s[18:19]
	global_load_ushort v71, v53, s[18:19]
	global_load_ushort v73, v50, s[18:19]
	v_lshl_or_b32 v50, v0, 2, v35
	v_ashrrev_i32_e32 v51, 31, v50
	v_lshl_add_u64 v[50:51], v[50:51], 3, s[36:37]
	global_load_dwordx2 v[96:97], v[50:51], off
	s_waitcnt vmcnt(18)
	v_cvt_f32_f16_e32 v0, v26
	v_sub_u32_e32 v54, v43, v42
	v_cmp_gt_i32_e32 vcc, v54, v58
	v_mov_b32_e32 v50, 0xff800000
	s_and_saveexec_b64 s[12:13], vcc
	s_cbranch_execz .LBB3_6
	s_waitcnt vmcnt(17)
	v_cvt_f32_f16_e32 v50, v48
	v_add_f32_e32 v50, v0, v50
	v_mul_f32_e32 v51, 0x3e4ccccd, v50
	v_max_f32_e32 v50, v50, v51
.LBB3_6:
	s_or_b64 exec, exec, s[12:13]
	v_cvt_f32_f16_sdwa v83, v26 dst_sel:DWORD dst_unused:UNUSED_PAD src0_sel:WORD_1
	s_waitcnt vmcnt(17)
	v_cvt_f32_f16_sdwa v26, v48 dst_sel:DWORD dst_unused:UNUSED_PAD src0_sel:WORD_1
	s_waitcnt vmcnt(15)
	v_cvt_f32_f16_e32 v52, v44
	v_cvt_f32_f16_e32 v84, v27
	v_cvt_f32_f16_sdwa v85, v27 dst_sel:DWORD dst_unused:UNUSED_PAD src0_sel:WORD_1
	v_cvt_f32_f16_e32 v27, v49
	v_cvt_f32_f16_sdwa v44, v44 dst_sel:DWORD dst_unused:UNUSED_PAD src0_sel:WORD_1
	v_cvt_f32_f16_sdwa v48, v49 dst_sel:DWORD dst_unused:UNUSED_PAD src0_sel:WORD_1
	v_cvt_f32_f16_e32 v53, v45
	v_cvt_f32_f16_e32 v49, v46
	v_cvt_f32_f16_sdwa v46, v46 dst_sel:DWORD dst_unused:UNUSED_PAD src0_sel:WORD_1
	v_cvt_f32_f16_e32 v51, v47
	v_cvt_f32_f16_sdwa v47, v47 dst_sel:DWORD dst_unused:UNUSED_PAD src0_sel:WORD_1
	v_cvt_f32_f16_sdwa v45, v45 dst_sel:DWORD dst_unused:UNUSED_PAD src0_sel:WORD_1
	s_waitcnt vmcnt(14)
	v_cvt_f32_f16_e32 v55, v28
	v_add_f32_e32 v26, v83, v26
	v_add_f32_e32 v52, v0, v52
	v_cvt_f32_f16_sdwa v28, v28 dst_sel:DWORD dst_unused:UNUSED_PAD src0_sel:WORD_1
	v_mul_f32_e32 v86, 0x3e4ccccd, v26
	v_add_f32_e32 v27, v84, v27
	v_mul_f32_e32 v90, 0x3e4ccccd, v52
	v_add_f32_e32 v44, v83, v44
	v_max_f32_e32 v26, v26, v86
	v_mul_f32_e32 v86, 0x3e4ccccd, v27
	v_add_f32_e32 v48, v85, v48
	v_max_f32_e32 v52, v52, v90
	v_mul_f32_e32 v90, 0x3e4ccccd, v44
	v_add_f32_e32 v53, v84, v53
	v_max_f32_e32 v27, v27, v86
	v_mul_f32_e32 v86, 0x3e4ccccd, v48
	v_add_f32_e32 v49, v0, v49
	v_add_f32_e32 v46, v83, v46
	v_add_f32_e32 v51, v84, v51
	v_add_f32_e32 v47, v85, v47
	v_max_f32_e32 v44, v44, v90
	v_mul_f32_e32 v90, 0x3e4ccccd, v53
	v_add_f32_e32 v45, v85, v45
	v_cvt_f32_f16_e32 v56, v29
	v_med3_i32 v57, v54, 0, 64
	v_max_f32_e32 v48, v48, v86
	v_mul_f32_e32 v86, 0x3e4ccccd, v49
	v_mul_f32_e32 v87, 0x3e4ccccd, v46
	v_mul_f32_e32 v88, 0x3e4ccccd, v51
	v_mul_f32_e32 v89, 0x3e4ccccd, v47
	v_max_f32_e32 v53, v53, v90
	v_mul_f32_e32 v90, 0x3e4ccccd, v45
	v_add_f32_e32 v55, v0, v55
	v_cvt_f32_f16_sdwa v29, v29 dst_sel:DWORD dst_unused:UNUSED_PAD src0_sel:WORD_1
	v_cndmask_b32_e32 v26, v77, v26, vcc
	v_cndmask_b32_e32 v27, v77, v27, vcc
	v_cndmask_b32_e32 v48, v77, v48, vcc
	v_max_f32_e32 v49, v49, v86
	v_cmp_lt_u32_e32 vcc, v59, v57
	v_max_f32_e32 v46, v46, v87
	v_max_f32_e32 v51, v51, v88
	v_max_f32_e32 v47, v47, v89
	v_max_f32_e32 v45, v45, v90
	v_mul_f32_e32 v90, 0x3e4ccccd, v55
	v_add_f32_e32 v28, v83, v28
	v_cndmask_b32_e32 v49, v77, v49, vcc
	v_cndmask_b32_e32 v46, v77, v46, vcc
	v_cndmask_b32_e32 v51, v77, v51, vcc
	v_cndmask_b32_e32 v47, v77, v47, vcc
	v_cmp_lt_u32_e32 vcc, v60, v57
	v_max_f32_e32 v55, v55, v90
	v_mul_f32_e32 v90, 0x3e4ccccd, v28
	v_cndmask_b32_e32 v52, v77, v52, vcc
	v_cndmask_b32_e32 v44, v77, v44, vcc
	v_cndmask_b32_e32 v53, v77, v53, vcc
	v_cndmask_b32_e32 v45, v77, v45, vcc
	v_cmp_lt_u32_e32 vcc, v61, v57
	v_max_f32_e32 v28, v28, v90
	v_max3_f32 v87, v26, s45, v46
	v_cndmask_b32_e32 v28, v77, v28, vcc
	v_add_f32_e32 v56, v84, v56
	v_max3_f32 v86, v50, s45, v49
	v_cndmask_b32_e32 v55, v77, v55, vcc
	v_max3_f32 v90, v87, v44, v28
	v_mul_f32_e32 v87, 0x3e4ccccd, v56
	v_add_f32_e32 v29, v85, v29
	v_max3_f32 v86, v86, v52, v55
	v_max_f32_e32 v56, v56, v87
	v_mul_f32_e32 v87, 0x3e4ccccd, v29
	v_max_f32_e32 v29, v29, v87
	v_cndmask_b32_e32 v56, v77, v56, vcc
	v_mov_b32_dpp v87, v86 quad_perm:[1,0,3,2] row_mask:0xf bank_mask:0xf bound_ctrl:1
	v_max_f32_e32 v87, v87, v87
	v_max_f32_e32 v86, v86, v87
	v_cndmask_b32_e32 v29, v77, v29, vcc
	v_max3_f32 v88, v27, s45, v51
	v_mov_b32_dpp v87, v86 quad_perm:[2,3,0,1] row_mask:0xf bank_mask:0xf bound_ctrl:1
	v_max_f32_e32 v87, v87, v87
	v_max_f32_e32 v86, v86, v87
	v_max3_f32 v88, v88, v53, v56
	v_max3_f32 v89, v48, s45, v47
	v_mov_b32_dpp v87, v86 row_half_mirror row_mask:0xf bank_mask:0xf bound_ctrl:1
	v_max_f32_e32 v87, v87, v87
	v_max_f32_e32 v86, v86, v87
	v_max3_f32 v89, v89, v45, v29
	v_readlane_b32 s14, v57, 32
	v_mov_b32_dpp v87, v86 row_mirror row_mask:0xf bank_mask:0xf bound_ctrl:1
	v_max3_f32 v86, v86, v87, s45
	v_cmp_neq_f32_e32 vcc, s45, v86
	v_readlane_b32 s15, v57, 48
	v_readlane_b32 s13, v57, 16
	v_cndmask_b32_e32 v87, 0, v86, vcc
	v_sub_f32_e32 v50, v50, v87
	v_sub_f32_e32 v49, v49, v87
	v_exp_f32_e32 v50, v50
	v_exp_f32_e32 v49, v49
	v_sub_f32_e32 v52, v52, v87
	v_sub_f32_e32 v55, v55, v87
	v_exp_f32_e32 v52, v52
	v_exp_f32_e32 v55, v55
	ds_write2_b32 v67, v50, v49 offset1:16
	ds_write2_b32 v67, v52, v55 offset0:32 offset1:48
	v_mov_b32_dpp v49, v90 quad_perm:[1,0,3,2] row_mask:0xf bank_mask:0xf bound_ctrl:1
	v_max_f32_e32 v49, v49, v49
	v_max_f32_e32 v49, v90, v49
	v_sub_f32_e32 v86, 0xff800000, v87
	v_exp_f32_e32 v86, v86
	v_mov_b32_dpp v50, v49 quad_perm:[2,3,0,1] row_mask:0xf bank_mask:0xf bound_ctrl:1
	v_max_f32_e32 v50, v50, v50
	v_max_f32_e32 v49, v49, v50
	s_max_i32 s14, s14, s15
	v_readlane_b32 s12, v57, 0
	v_mov_b32_dpp v50, v49 row_half_mirror row_mask:0xf bank_mask:0xf bound_ctrl:1
	v_max_f32_e32 v50, v50, v50
	v_max_f32_e32 v49, v49, v50
	s_nop 1
	v_mov_b32_dpp v50, v49 row_mirror row_mask:0xf bank_mask:0xf bound_ctrl:1
	v_max3_f32 v49, v49, v50, s45
	v_cmp_neq_f32_e32 vcc, s45, v49
	v_cndmask_b32_e64 v50, 0, v86, s[0:1]
	s_nop 0
	v_cndmask_b32_e32 v90, 0, v49, vcc
	v_sub_f32_e32 v26, v26, v90
	v_sub_f32_e32 v46, v46, v90
	v_sub_f32_e32 v28, v28, v90
	v_exp_f32_e32 v26, v26
	v_exp_f32_e32 v46, v46
	v_sub_f32_e32 v44, v44, v90
	v_exp_f32_e32 v28, v28
	v_exp_f32_e32 v44, v44
	ds_write2_b32 v67, v26, v46 offset0:68 offset1:84
	ds_write2_b32 v67, v44, v28 offset0:100 offset1:116
	v_mov_b32_dpp v28, v88 quad_perm:[1,0,3,2] row_mask:0xf bank_mask:0xf bound_ctrl:1
	v_max_f32_e32 v28, v28, v28
	v_max_f32_e32 v28, v88, v28
	v_sub_f32_e32 v49, 0xff800000, v90
	v_exp_f32_e32 v49, v49
	v_mov_b32_dpp v44, v28 quad_perm:[2,3,0,1] row_mask:0xf bank_mask:0xf bound_ctrl:1
	v_max_f32_e32 v44, v44, v44
	v_max_f32_e32 v28, v28, v44
	v_cndmask_b32_e64 v26, v50, v49, s[2:3]
	s_nop 0
	v_mov_b32_dpp v44, v28 row_half_mirror row_mask:0xf bank_mask:0xf bound_ctrl:1
	v_max_f32_e32 v44, v44, v44
	v_max_f32_e32 v28, v28, v44
	s_nop 1
	v_mov_b32_dpp v44, v28 row_mirror row_mask:0xf bank_mask:0xf bound_ctrl:1
	v_max3_f32 v28, v28, v44, s45
	v_cmp_neq_f32_e32 vcc, s45, v28
	s_nop 1
	v_cndmask_b32_e32 v86, 0, v28, vcc
	v_sub_f32_e32 v27, v27, v86
	v_sub_f32_e32 v28, v51, v86
	v_exp_f32_e32 v27, v27
	v_exp_f32_e32 v28, v28
	v_sub_f32_e32 v44, v53, v86
	v_sub_f32_e32 v46, v56, v86
	v_exp_f32_e32 v44, v44
	v_exp_f32_e32 v46, v46
	ds_write2_b32 v67, v27, v28 offset0:136 offset1:152
	ds_write2_b32 v67, v44, v46 offset0:168 offset1:184
	v_mov_b32_dpp v27, v89 quad_perm:[1,0,3,2] row_mask:0xf bank_mask:0xf bound_ctrl:1
	v_max_f32_e32 v27, v27, v27
	v_max_f32_e32 v27, v89, v27
	v_sub_f32_e32 v49, 0xff800000, v86
	v_exp_f32_e32 v49, v49
	v_mov_b32_dpp v28, v27 quad_perm:[2,3,0,1] row_mask:0xf bank_mask:0xf bound_ctrl:1
	v_max_f32_e32 v28, v28, v28
	v_max_f32_e32 v27, v27, v28
	v_cndmask_b32_e64 v26, v26, v49, s[4:5]
	s_nop 0
	v_mov_b32_dpp v28, v27 row_half_mirror row_mask:0xf bank_mask:0xf bound_ctrl:1
	v_max_f32_e32 v28, v28, v28
	v_max_f32_e32 v27, v27, v28
	s_nop 1
	v_mov_b32_dpp v28, v27 row_mirror row_mask:0xf bank_mask:0xf bound_ctrl:1
	v_max3_f32 v27, v27, v28, s45
	v_cmp_neq_f32_e32 vcc, s45, v27
	s_nop 1
	v_cndmask_b32_e32 v89, 0, v27, vcc
	v_sub_f32_e32 v27, 0xff800000, v89
	v_sub_f32_e32 v28, v48, v89
	v_sub_f32_e32 v44, v47, v89
	v_exp_f32_e32 v27, v27
	v_exp_f32_e32 v28, v28
	v_exp_f32_e32 v44, v44
	v_sub_f32_e32 v45, v45, v89
	v_sub_f32_e32 v29, v29, v89
	v_exp_f32_e32 v45, v45
	v_exp_f32_e32 v29, v29
	v_cndmask_b32_e64 v26, v26, v27, s[6:7]
	ds_write2_b32 v67, v28, v44 offset0:204 offset1:220
	ds_write2_b32 v67, v45, v29 offset0:236 offset1:252
	v_mul_f32_e32 v45, 0, v26
	v_mov_b32_e32 v26, s13
	v_mov_b32_e32 v27, s14
	v_max3_i32 v26, s12, v26, v27
	v_cmp_gt_i32_e32 vcc, 1, v26
	v_readfirstlane_b32 s12, v26
	s_cbranch_vccnz .LBB3_12
	s_add_i32 s12, s12, 3
	s_ashr_i32 s13, s12, 31
	s_lshr_b32 s13, s13, 30
	s_add_i32 s12, s12, s13
	s_ashr_i32 s12, s12, 2
	s_max_i32 s13, s12, 1
	s_mov_b32 s14, 0
	v_mov_b32_e32 v52, v64
	v_mov_b32_e32 v55, v65
	v_mov_b32_e32 v50, v45
	v_mov_b32_e32 v51, v45
	v_mov_b32_e32 v48, v45
	v_mov_b32_e32 v49, v45
	v_mov_b32_e32 v46, v45
	v_mov_b32_e32 v47, v45
	v_mov_b32_e32 v44, v45
	v_mov_b32_e32 v53, v45
.Lagg1_ring:
	s_add_i32 s15, s14, 2
	s_cmp_lt_i32 s15, s12
	s_cbranch_scc0 .Lagg1_drain_a
	ds_read_b128 v[26:29], v55
	ds_read_b128 v[98:101], v52 offset:32
	s_waitcnt lgkmcnt(0)
	v_add_u32_e32 v98, v98, v30
	v_add_u32_e32 v99, v99, v30
	v_add_u32_e32 v100, v100, v30
	v_add_u32_e32 v101, v101, v30
	s_waitcnt vmcnt(7)
	v_fma_mix_f32 v48, v10, v26, v48 op_sel_hi:[1,0,0]
	v_fma_mix_f32 v51, v10, v26, v51 op_sel:[1,0,0] op_sel_hi:[1,0,0]
	v_fma_mix_f32 v50, v11, v26, v50 op_sel_hi:[1,0,0]
	v_fma_mix_f32 v45, v11, v26, v45 op_sel:[1,0,0] op_sel_hi:[1,0,0]
	v_fma_mix_f32 v49, v12, v26, v49 op_sel_hi:[1,0,0]
	v_fma_mix_f32 v46, v12, v26, v46 op_sel:[1,0,0] op_sel_hi:[1,0,0]
	v_fma_mix_f32 v47, v13, v26, v47 op_sel_hi:[1,0,0]
	v_fma_mix_f32 v44, v13, v26, v44 op_sel:[1,0,0] op_sel_hi:[1,0,0]
	global_load_dwordx4 v[10:13], v98, s[20:21]
	s_waitcnt vmcnt(7)
	v_fma_mix_f32 v48, v14, v27, v48 op_sel_hi:[1,0,0]
	v_fma_mix_f32 v51, v14, v27, v51 op_sel:[1,0,0] op_sel_hi:[1,0,0]
	v_fma_mix_f32 v50, v15, v27, v50 op_sel_hi:[1,0,0]
	v_fma_mix_f32 v45, v15, v27, v45 op_sel:[1,0,0] op_sel_hi:[1,0,0]
	v_fma_mix_f32 v49, v16, v27, v49 op_sel_hi:[1,0,0]
	v_fma_mix_f32 v46, v16, v27, v46 op_sel:[1,0,0] op_sel_hi:[1,0,0]
	v_fma_mix_f32 v47, v17, v27, v47 op_sel_hi:[1,0,0]
	v_fma_mix_f32 v44, v17, v27, v44 op_sel:[1,0,0] op_sel_hi:[1,0,0]
	global_load_dwordx4 v[14:17], v99, s[20:21]
	s_waitcnt vmcnt(7)
	v_fma_mix_f32 v48, v18, v28, v48 op_sel_hi:[1,0,0]
	v_fma_mix_f32 v51, v18, v28, v51 op_sel:[1,0,0] op_sel_hi:[1,0,0]
	v_fma_mix_f32 v50, v19, v28, v50 op_sel_hi:[1,0,0]
	v_fma_mix_f32 v45, v19, v28, v45 op_sel:[1,0,0] op_sel_hi:[1,0,0]
	v_fma_mix_f32 v49, v20, v28, v49 op_sel_hi:[1,0,0]
	v_fma_mix_f32 v46, v20, v28, v46 op_sel:[1,0,0] op_sel_hi:[1,0,0]
	v_fma_mix_f32 v47, v21, v28, v47 op_sel_hi:[1,0,0]
	v_fma_mix_f32 v44, v21, v28, v44 op_sel:[1,0,0] op_sel_hi:[1,0,0]
	global_load_dwordx4 v[18:21], v100, s[20:21]
	s_waitcnt vmcnt(7)
	v_fma_mix_f32 v48, v22, v29, v48 op_sel_hi:[1,0,0]
	v_fma_mix_f32 v51, v22, v29, v51 op_sel:[1,0,0] op_sel_hi:[1,0,0]
	v_fma_mix_f32 v50, v23, v29, v50 op_sel_hi:[1,0,0]
	v_fma_mix_f32 v45, v23, v29, v45 op_sel:[1,0,0] op_sel_hi:[1,0,0]
	v_fma_mix_f32 v49, v24, v29, v49 op_sel_hi:[1,0,0]
	v_fma_mix_f32 v46, v24, v29, v46 op_sel:[1,0,0] op_sel_hi:[1,0,0]
	v_fma_mix_f32 v47, v25, v29, v47 op_sel_hi:[1,0,0]
	v_fma_mix_f32 v44, v25, v29, v44 op_sel:[1,0,0] op_sel_hi:[1,0,0]
	global_load_dwordx4 v[22:25], v101, s[20:21]
	v_add_f32_e32 v56, v26, v27
	v_add_f32_e32 v57, v28, v29
	v_add_f32_e32 v56, v56, v57
	v_add_f32_e32 v53, v53, v56
	s_add_i32 s15, s14, 3
	s_cmp_lt_i32 s15, s12
	s_cbranch_scc0 .Lagg1_drain_b
	ds_read_b128 v[26:29], v55 offset:16
	ds_read_b128 v[98:101], v52 offset:48
	s_waitcnt lgkmcnt(0)
	v_add_u32_e32 v98, v98, v30
	v_add_u32_e32 v99, v99, v30
	v_add_u32_e32 v100, v100, v30
	v_add_u32_e32 v101, v101, v30
	s_waitcnt vmcnt(7)
	v_fma_mix_f32 v48, v110, v26, v48 op_sel_hi:[1,0,0]
	v_fma_mix_f32 v51, v110, v26, v51 op_sel:[1,0,0] op_sel_hi:[1,0,0]
	v_fma_mix_f32 v50, v111, v26, v50 op_sel_hi:[1,0,0]
	v_fma_mix_f32 v45, v111, v26, v45 op_sel:[1,0,0] op_sel_hi:[1,0,0]
	v_fma_mix_f32 v49, v112, v26, v49 op_sel_hi:[1,0,0]
	v_fma_mix_f32 v46, v112, v26, v46 op_sel:[1,0,0] op_sel_hi:[1,0,0]
	v_fma_mix_f32 v47, v113, v26, v47 op_sel_hi:[1,0,0]
	v_fma_mix_f32 v44, v113, v26, v44 op_sel:[1,0,0] op_sel_hi:[1,0,0]
	global_load_dwordx4 v[110:113], v98, s[20:21]
	s_waitcnt vmcnt(7)
	v_fma_mix_f32 v48, v114, v27, v48 op_sel_hi:[1,0,0]
	v_fma_mix_f32 v51, v114, v27, v51 op_sel:[1,0,0] op_sel_hi:[1,0,0]
	v_fma_mix_f32 v50, v115, v27, v50 op_sel_hi:[1,0,0]
	v_fma_mix_f32 v45, v115, v27, v45 op_sel:[1,0,0] op_sel_hi:[1,0,0]
	v_fma_mix_f32 v49, v116, v27, v49 op_sel_hi:[1,0,0]
	v_fma_mix_f32 v46, v116, v27, v46 op_sel:[1,0,0] op_sel_hi:[1,0,0]
	v_fma_mix_f32 v47, v117, v27, v47 op_sel_hi:[1,0,0]
	v_fma_mix_f32 v44, v117, v27, v44 op_sel:[1,0,0] op_sel_hi:[1,0,0]
	global_load_dwordx4 v[114:117], v99, s[20:21]
	s_waitcnt vmcnt(7)
	v_fma_mix_f32 v48, v118, v28, v48 op_sel_hi:[1,0,0]
	v_fma_mix_f32 v51, v118, v28, v51 op_sel:[1,0,0] op_sel_hi:[1,0,0]
	v_fma_mix_f32 v50, v119, v28, v50 op_sel_hi:[1,0,0]
	v_fma_mix_f32 v45, v119, v28, v45 op_sel:[1,0,0] op_sel_hi:[1,0,0]
	v_fma_mix_f32 v49, v120, v28, v49 op_sel_hi:[1,0,0]
	v_fma_mix_f32 v46, v120, v28, v46 op_sel:[1,0,0] op_sel_hi:[1,0,0]
	v_fma_mix_f32 v47, v121, v28, v47 op_sel_hi:[1,0,0]
	v_fma_mix_f32 v44, v121, v28, v44 op_sel:[1,0,0] op_sel_hi:[1,0,0]
	global_load_dwordx4 v[118:121], v100, s[20:21]
	s_waitcnt vmcnt(7)
	v_fma_mix_f32 v48, v122, v29, v48 op_sel_hi:[1,0,0]
	v_fma_mix_f32 v51, v122, v29, v51 op_sel:[1,0,0] op_sel_hi:[1,0,0]
	v_fma_mix_f32 v50, v123, v29, v50 op_sel_hi:[1,0,0]
	v_fma_mix_f32 v45, v123, v29, v45 op_sel:[1,0,0] op_sel_hi:[1,0,0]
	v_fma_mix_f32 v49, v124, v29, v49 op_sel_hi:[1,0,0]
	v_fma_mix_f32 v46, v124, v29, v46 op_sel:[1,0,0] op_sel_hi:[1,0,0]
	v_fma_mix_f32 v47, v125, v29, v47 op_sel_hi:[1,0,0]
	v_fma_mix_f32 v44, v125, v29, v44 op_sel:[1,0,0] op_sel_hi:[1,0,0]
	global_load_dwordx4 v[122:125], v101, s[20:21]
	v_add_f32_e32 v56, v26, v27
	v_add_f32_e32 v57, v28, v29
	v_add_f32_e32 v56, v56, v57
	v_add_f32_e32 v53, v53, v56
	s_add_i32 s14, s14, 2
	v_add_u32_e32 v55, 32, v55
	v_add_u32_e32 v52, 32, v52
	s_branch .Lagg1_ring
.Lagg1_drain_a:
	ds_read_b128 v[26:29], v55
	s_add_i32 s15, s14, 1
	s_cmp_lt_i32 s15, s12
	s_cbranch_scc1 .Lagg1_drain_a4
	s_waitcnt vmcnt(0)
.Lagg1_drain_a4:
	s_waitcnt vmcnt(4) lgkmcnt(0)
	v_fma_mix_f32 v48, v10, v26, v48 op_sel_hi:[1,0,0]
	v_fma_mix_f32 v51, v10, v26, v51 op_sel:[1,0,0] op_sel_hi:[1,0,0]
	v_fma_mix_f32 v50, v11, v26, v50 op_sel_hi:[1,0,0]
	v_fma_mix_f32 v45, v11, v26, v45 op_sel:[1,0,0] op_sel_hi:[1,0,0]
	v_fma_mix_f32 v49, v12, v26, v49 op_sel_hi:[1,0,0]
	v_fma_mix_f32 v46, v12, v26, v46 op_sel:[1,0,0] op_sel_hi:[1,0,0]
	v_fma_mix_f32 v47, v13, v26, v47 op_sel_hi:[1,0,0]
	v_fma_mix_f32 v44, v13, v26, v44 op_sel:[1,0,0] op_sel_hi:[1,0,0]
	v_fma_mix_f32 v48, v14, v27, v48 op_sel_hi:[1,0,0]
	v_fma_mix_f32 v51, v14, v27, v51 op_sel:[1,0,0] op_sel_hi:[1,0,0]
	v_fma_mix_f32 v50, v15, v27, v50 op_sel_hi:[1,0,0]
	v_fma_mix_f32 v45, v15, v27, v45 op_sel:[1,0,0] op_sel_hi:[1,0,0]
	v_fma_mix_f32 v49, v16, v27, v49 op_sel_hi:[1,0,0]
	v_fma_mix_f32 v46, v16, v27, v46 op_sel:[1,0,0] op_sel_hi:[1,0,0]
	v_fma_mix_f32 v47, v17, v27, v47 op_sel_hi:[1,0,0]
	v_fma_mix_f32 v44, v17, v27, v44 op_sel:[1,0,0] op_sel_hi:[1,0,0]
	v_fma_mix_f32 v48, v18, v28, v48 op_sel_hi:[1,0,0]
	v_fma_mix_f32 v51, v18, v28, v51 op_sel:[1,0,0] op_sel_hi:[1,0,0]
	v_fma_mix_f32 v50, v19, v28, v50 op_sel_hi:[1,0,0]
	v_fma_mix_f32 v45, v19, v28, v45 op_sel:[1,0,0] op_sel_hi:[1,0,0]
	v_fma_mix_f32 v49, v20, v28, v49 op_sel_hi:[1,0,0]
	v_fma_mix_f32 v46, v20, v28, v46 op_sel:[1,0,0] op_sel_hi:[1,0,0]
	v_fma_mix_f32 v47, v21, v28, v47 op_sel_hi:[1,0,0]
	v_fma_mix_f32 v44, v21, v28, v44 op_sel:[1,0,0] op_sel_hi:[1,0,0]
	v_fma_mix_f32 v48, v22, v29, v48 op_sel_hi:[1,0,0]
	v_fma_mix_f32 v51, v22, v29, v51 op_sel:[1,0,0] op_sel_hi:[1,0,0]
	v_fma_mix_f32 v50, v23, v29, v50 op_sel_hi:[1,0,0]
	v_fma_mix_f32 v45, v23, v29, v45 op_sel:[1,0,0] op_sel_hi:[1,0,0]
	v_fma_mix_f32 v49, v24, v29, v49 op_sel_hi:[1,0,0]
	v_fma_mix_f32 v46, v24, v29, v46 op_sel:[1,0,0] op_sel_hi:[1,0,0]
	v_fma_mix_f32 v47, v25, v29, v47 op_sel_hi:[1,0,0]
	v_fma_mix_f32 v44, v25, v29, v44 op_sel:[1,0,0] op_sel_hi:[1,0,0]
	v_add_f32_e32 v56, v26, v27
	v_add_f32_e32 v57, v28, v29
	v_add_f32_e32 v56, v56, v57
	v_add_f32_e32 v53, v53, v56
	s_cbranch_scc0 .Lagg1_ring_done
	ds_read_b128 v[26:29], v55 offset:16
	s_waitcnt vmcnt(0) lgkmcnt(0)
	v_fma_mix_f32 v48, v110, v26, v48 op_sel_hi:[1,0,0]
	v_fma_mix_f32 v51, v110, v26, v51 op_sel:[1,0,0] op_sel_hi:[1,0,0]
	v_fma_mix_f32 v50, v111, v26, v50 op_sel_hi:[1,0,0]
	v_fma_mix_f32 v45, v111, v26, v45 op_sel:[1,0,0] op_sel_hi:[1,0,0]
	v_fma_mix_f32 v49, v112, v26, v49 op_sel_hi:[1,0,0]
	v_fma_mix_f32 v46, v112, v26, v46 op_sel:[1,0,0] op_sel_hi:[1,0,0]
	v_fma_mix_f32 v47, v113, v26, v47 op_sel_hi:[1,0,0]
	v_fma_mix_f32 v44, v113, v26, v44 op_sel:[1,0,0] op_sel_hi:[1,0,0]
	v_fma_mix_f32 v48, v114, v27, v48 op_sel_hi:[1,0,0]
	v_fma_mix_f32 v51, v114, v27, v51 op_sel:[1,0,0] op_sel_hi:[1,0,0]
	v_fma_mix_f32 v50, v115, v27, v50 op_sel_hi:[1,0,0]
	v_fma_mix_f32 v45, v115, v27, v45 op_sel:[1,0,0] op_sel_hi:[1,0,0]
	v_fma_mix_f32 v49, v116, v27, v49 op_sel_hi:[1,0,0]
	v_fma_mix_f32 v46, v116, v27, v46 op_sel:[1,0,0] op_sel_hi:[1,0,0]
	v_fma_mix_f32 v47, v117, v27, v47 op_sel_hi:[1,0,0]
	v_fma_mix_f32 v44, v117, v27, v44 op_sel:[1,0,0] op_sel_hi:[1,0,0]
	v_fma_mix_f32 v48, v118, v28, v48 op_sel_hi:[1,0,0]
	v_fma_mix_f32 v51, v118, v28, v51 op_sel:[1,0,0] op_sel_hi:[1,0,0]
	v_fma_mix_f32 v50, v119, v28, v50 op_sel_hi:[1,0,0]
	v_fma_mix_f32 v45, v119, v28, v45 op_sel:[1,0,0] op_sel_hi:[1,0,0]
	v_fma_mix_f32 v49, v120, v28, v49 op_sel_hi:[1,0,0]
	v_fma_mix_f32 v46, v120, v28, v46 op_sel:[1,0,0] op_sel_hi:[1,0,0]
	v_fma_mix_f32 v47, v121, v28, v47 op_sel_hi:[1,0,0]
	v_fma_mix_f32 v44, v121, v28, v44 op_sel:[1,0,0] op_sel_hi:[1,0,0]
	v_fma_mix_f32 v48, v122, v29, v48 op_sel_hi:[1,0,0]
	v_fma_mix_f32 v51, v122, v29, v51 op_sel:[1,0,0] op_sel_hi:[1,0,0]
	v_fma_mix_f32 v50, v123, v29, v50 op_sel_hi:[1,0,0]
	v_fma_mix_f32 v45, v123, v29, v45 op_sel:[1,0,0] op_sel_hi:[1,0,0]
	v_fma_mix_f32 v49, v124, v29, v49 op_sel_hi:[1,0,0]
	v_fma_mix_f32 v46, v124, v29, v46 op_sel:[1,0,0] op_sel_hi:[1,0,0]
	v_fma_mix_f32 v47, v125, v29, v47 op_sel_hi:[1,0,0]
	v_fma_mix_f32 v44, v125, v29, v44 op_sel:[1,0,0] op_sel_hi:[1,0,0]
	v_add_f32_e32 v56, v26, v27
	v_add_f32_e32 v57, v28, v29
	v_add_f32_e32 v56, v56, v57
	v_add_f32_e32 v53, v53, v56
	s_branch .Lagg1_ring_done
.Lagg1_drain_b:
	ds_read_b128 v[26:29], v55 offset:16
	s_waitcnt vmcnt(4) lgkmcnt(0)
	v_fma_mix_f32 v48, v110, v26, v48 op_sel_hi:[1,0,0]
	v_fma_mix_f32 v51, v110, v26, v51 op_sel:[1,0,0] op_sel_hi:[1,0,0]
	v_fma_mix_f32 v50, v111, v26, v50 op_sel_hi:[1,0,0]
	v_fma_mix_f32 v45, v111, v26, v45 op_sel:[1,0,0] op_sel_hi:[1,0,0]
	v_fma_mix_f32 v49, v112, v26, v49 op_sel_hi:[1,0,0]
	v_fma_mix_f32 v46, v112, v26, v46 op_sel:[1,0,0] op_sel_hi:[1,0,0]
	v_fma_mix_f32 v47, v113, v26, v47 op_sel_hi:[1,0,0]
	v_fma_mix_f32 v44, v113, v26, v44 op_sel:[1,0,0] op_sel_hi:[1,0,0]
	v_fma_mix_f32 v48, v114, v27, v48 op_sel_hi:[1,0,0]
	v_fma_mix_f32 v51, v114, v27, v51 op_sel:[1,0,0] op_sel_hi:[1,0,0]
	v_fma_mix_f32 v50, v115, v27, v50 op_sel_hi:[1,0,0]
	v_fma_mix_f32 v45, v115, v27, v45 op_sel:[1,0,0] op_sel_hi:[1,0,0]
	v_fma_mix_f32 v49, v116, v27, v49 op_sel_hi:[1,0,0]
	v_fma_mix_f32 v46, v116, v27, v46 op_sel:[1,0,0] op_sel_hi:[1,0,0]
	v_fma_mix_f32 v47, v117, v27, v47 op_sel_hi:[1,0,0]
	v_fma_mix_f32 v44, v117, v27, v44 op_sel:[1,0,0] op_sel_hi:[1,0,0]
	v_fma_mix_f32 v48, v118, v28, v48 op_sel_hi:[1,0,0]
	v_fma_mix_f32 v51, v118, v28, v51 op_sel:[1,0,0] op_sel_hi:[1,0,0]
	v_fma_mix_f32 v50, v119, v28, v50 op_sel_hi:[1,0,0]
	v_fma_mix_f32 v45, v119, v28, v45 op_sel:[1,0,0] op_sel_hi:[1,0,0]
	v_fma_mix_f32 v49, v120, v28, v49 op_sel_hi:[1,0,0]
	v_fma_mix_f32 v46, v120, v28, v46 op_sel:[1,0,0] op_sel_hi:[1,0,0]
	v_fma_mix_f32 v47, v121, v28, v47 op_sel_hi:[1,0,0]
	v_fma_mix_f32 v44, v121, v28, v44 op_sel:[1,0,0] op_sel_hi:[1,0,0]
	v_fma_mix_f32 v48, v122, v29, v48 op_sel_hi:[1,0,0]
	v_fma_mix_f32 v51, v122, v29, v51 op_sel:[1,0,0] op_sel_hi:[1,0,0]
	v_fma_mix_f32 v50, v123, v29, v50 op_sel_hi:[1,0,0]
	v_fma_mix_f32 v45, v123, v29, v45 op_sel:[1,0,0] op_sel_hi:[1,0,0]
	v_fma_mix_f32 v49, v124, v29, v49 op_sel_hi:[1,0,0]
	v_fma_mix_f32 v46, v124, v29, v46 op_sel:[1,0,0] op_sel_hi:[1,0,0]
	v_fma_mix_f32 v47, v125, v29, v47 op_sel_hi:[1,0,0]
	v_fma_mix_f32 v44, v125, v29, v44 op_sel:[1,0,0] op_sel_hi:[1,0,0]
	v_add_f32_e32 v56, v26, v27
	v_add_f32_e32 v57, v28, v29
	v_add_f32_e32 v56, v56, v57
	v_add_f32_e32 v53, v53, v56
	ds_read_b128 v[26:29], v55 offset:32
	s_waitcnt vmcnt(0) lgkmcnt(0)
	v_fma_mix_f32 v48, v10, v26, v48 op_sel_hi:[1,0,0]
	v_fma_mix_f32 v51, v10, v26, v51 op_sel:[1,0,0] op_sel_hi:[1,0,0]
	v_fma_mix_f32 v50, v11, v26, v50 op_sel_hi:[1,0,0]
	v_fma_mix_f32 v45, v11, v26, v45 op_sel:[1,0,0] op_sel_hi:[1,0,0]
	v_fma_mix_f32 v49, v12, v26, v49 op_sel_hi:[1,0,0]
	v_fma_mix_f32 v46, v12, v26, v46 op_sel:[1,0,0] op_sel_hi:[1,0,0]
	v_fma_mix_f32 v47, v13, v26, v47 op_sel_hi:[1,0,0]
	v_fma_mix_f32 v44, v13, v26, v44 op_sel:[1,0,0] op_sel_hi:[1,0,0]
	v_fma_mix_f32 v48, v14, v27, v48 op_sel_hi:[1,0,0]
	v_fma_mix_f32 v51, v14, v27, v51 op_sel:[1,0,0] op_sel_hi:[1,0,0]
	v_fma_mix_f32 v50, v15, v27, v50 op_sel_hi:[1,0,0]
	v_fma_mix_f32 v45, v15, v27, v45 op_sel:[1,0,0] op_sel_hi:[1,0,0]
	v_fma_mix_f32 v49, v16, v27, v49 op_sel_hi:[1,0,0]
	v_fma_mix_f32 v46, v16, v27, v46 op_sel:[1,0,0] op_sel_hi:[1,0,0]
	v_fma_mix_f32 v47, v17, v27, v47 op_sel_hi:[1,0,0]
	v_fma_mix_f32 v44, v17, v27, v44 op_sel:[1,0,0] op_sel_hi:[1,0,0]
	v_fma_mix_f32 v48, v18, v28, v48 op_sel_hi:[1,0,0]
	v_fma_mix_f32 v51, v18, v28, v51 op_sel:[1,0,0] op_sel_hi:[1,0,0]
	v_fma_mix_f32 v50, v19, v28, v50 op_sel_hi:[1,0,0]
	v_fma_mix_f32 v45, v19, v28, v45 op_sel:[1,0,0] op_sel_hi:[1,0,0]
	v_fma_mix_f32 v49, v20, v28, v49 op_sel_hi:[1,0,0]
	v_fma_mix_f32 v46, v20, v28, v46 op_sel:[1,0,0] op_sel_hi:[1,0,0]
	v_fma_mix_f32 v47, v21, v28, v47 op_sel_hi:[1,0,0]
	v_fma_mix_f32 v44, v21, v28, v44 op_sel:[1,0,0] op_sel_hi:[1,0,0]
	v_fma_mix_f32 v48, v22, v29, v48 op_sel_hi:[1,0,0]
	v_fma_mix_f32 v51, v22, v29, v51 op_sel:[1,0,0] op_sel_hi:[1,0,0]
	v_fma_mix_f32 v50, v23, v29, v50 op_sel_hi:[1,0,0]
	v_fma_mix_f32 v45, v23, v29, v45 op_sel:[1,0,0] op_sel_hi:[1,0,0]
	v_fma_mix_f32 v49, v24, v29, v49 op_sel_hi:[1,0,0]
	v_fma_mix_f32 v46, v24, v29, v46 op_sel:[1,0,0] op_sel_hi:[1,0,0]
	v_fma_mix_f32 v47, v25, v29, v47 op_sel_hi:[1,0,0]
	v_fma_mix_f32 v44, v25, v29, v44 op_sel:[1,0,0] op_sel_hi:[1,0,0]
	v_add_f32_e32 v56, v26, v27
	v_add_f32_e32 v57, v28, v29
	v_add_f32_e32 v56, v56, v57
	v_add_f32_e32 v53, v53, v56
.Lagg1_ring_done:
.LBB3_11:
	v_mov_b32_e32 v52, v45
	v_mov_b32_e32 v45, v44
	s_branch .LBB3_13

.LBB3_24:
	v_div_scale_f32 v0, s[12:13], v53, v53, 1.0
	s_waitcnt vmcnt(3)
	v_rcp_f32_e32 v10, v0
	v_div_scale_f32 v11, vcc, 1.0, v53, 1.0
	v_mov_b32_e32 v44, v47
	v_fma_f32 v12, -v0, v10, 1.0
	v_fmac_f32_e32 v10, v12, v10
	v_mul_f32_e32 v12, v11, v10
	v_fma_f32 v13, -v0, v12, v11
	v_fmac_f32_e32 v12, v13, v10
	v_fma_f32 v0, -v0, v12, v11
	v_div_fmas_f32 v0, v0, v10, v12
	v_div_fixup_f32 v0, v0, v53, 1.0
	v_cmp_lt_f32_e32 vcc, 0, v53
	v_mov_b32_e32 v10, v48
	v_mov_b32_e32 v11, v51
	v_cndmask_b32_e32 v0, 0, v0, vcc
	v_pk_fma_f32 v[10:11], v[10:11], v[0:1], v[6:7] op_sel_hi:[1,0,1]
	v_mov_b32_e32 v51, v52
	v_mul_f32_e32 v12, 0x3fb8aa3b, v10
	v_mul_f32_e32 v13, 0x3fb8aa3b, v11
	v_exp_f32_e32 v12, v12
	v_exp_f32_e32 v13, v13
	v_cmp_lt_f32_e32 vcc, 0, v11
	s_waitcnt vmcnt(2)
	v_pk_fma_f32 v[14:15], v[50:51], v[0:1], v[8:9] op_sel_hi:[1,0,1]
	v_pk_add_f32 v[12:13], v[12:13], -1.0 op_sel_hi:[1,0]
	s_nop 0
	v_cndmask_b32_e32 v11, v13, v11, vcc
	v_mul_f32_e32 v13, 0x3fb8aa3b, v14
	v_exp_f32_e32 v16, v13
	v_mul_f32_e32 v13, 0x3fb8aa3b, v15
	v_exp_f32_e32 v17, v13
	v_cmp_lt_f32_e32 vcc, 0, v10
	s_nop 1
	v_cndmask_b32_e32 v10, v12, v10, vcc
	v_pk_add_f32 v[12:13], v[16:17], -1.0 op_sel_hi:[1,0]
	v_pk_mov_b32 v[16:17], v[48:49], v[46:47] op_sel:[1,0]
	v_cmp_lt_f32_e32 vcc, 0, v15
	v_pk_fma_f32 v[16:17], v[16:17], v[0:1], v[2:3] op_sel_hi:[1,0,1]
	v_cvt_pk_f16_f32 v10, v10, v11
	v_cndmask_b32_e32 v11, v13, v15, vcc
	v_mul_f32_e32 v13, 0x3fb8aa3b, v16
	s_waitcnt vmcnt(1)
	v_exp_f32_e32 v18, v13
	v_mul_f32_e32 v13, 0x3fb8aa3b, v17
	v_exp_f32_e32 v19, v13
	v_cmp_lt_f32_e32 vcc, 0, v14
	s_nop 1
	v_cndmask_b32_e32 v12, v12, v14, vcc
	v_pk_fma_f32 v[14:15], v[44:45], v[0:1], v[4:5] op_sel_hi:[1,0,1]
	v_cvt_pk_f16_f32 v11, v12, v11
	v_mul_f32_e32 v0, 0x3fb8aa3b, v14
	v_pk_add_f32 v[12:13], v[18:19], -1.0 op_sel_hi:[1,0]
	v_exp_f32_e32 v18, v0
	v_mul_f32_e32 v0, 0x3fb8aa3b, v15
	v_exp_f32_e32 v19, v0
	v_cmp_lt_f32_e32 vcc, 0, v17
	s_nop 1
	v_cndmask_b32_e32 v13, v13, v17, vcc
	v_cmp_lt_f32_e32 vcc, 0, v16
	s_nop 1
	v_cndmask_b32_e32 v0, v12, v16, vcc
	v_pk_add_f32 v[16:17], v[18:19], -1.0 op_sel_hi:[1,0]
	v_cmp_lt_f32_e32 vcc, 0, v15
	v_cvt_pk_f16_f32 v12, v0, v13
	s_nop 0
	v_cndmask_b32_e32 v0, v17, v15, vcc
	v_cmp_lt_f32_e32 vcc, 0, v14
	s_nop 1
	v_cndmask_b32_e32 v13, v16, v14, vcc
	v_cvt_pk_f16_f32 v13, v13, v0
	v_lshl_or_b32 v0, v82, 2, v35
	v_cmp_eq_u32_e32 vcc, 0, v82
	v_mad_u64_u32 v[14:15], s[12:13], v0, s39, v[32:33]
	s_nop 0
	v_cndmask_b32_e32 v81, v81, v33, vcc
	v_add_u32_e32 v0, 1, v82
	v_add_u32_e32 v33, s33, v33
	v_cmp_eq_u32_e64 s[12:13], 4, v0
	v_cmp_lt_i32_e32 vcc, s38, v33
	s_or_b64 s[12:13], s[12:13], vcc
	ds_write_b128 v14, v[10:13]
	s_and_saveexec_b64 s[28:29], s[12:13]
	s_cbranch_execz .LBB3_3
	v_mov_b32_e32 v117, 0
	v_mov_b32_e32 v116, 0
	v_mov_b32_e32 v115, 0
	v_mov_b32_e32 v114, 0
	v_mov_b32_e32 v113, 0
	v_mov_b32_e32 v112, 0
	v_mov_b32_e32 v111, 0
	v_mov_b32_e32 v110, 0
	v_mov_b32_e32 v121, 0
	v_mov_b32_e32 v120, 0
	v_mov_b32_e32 v119, 0
	v_mov_b32_e32 v118, 0
	s_mov_b32 s12, 0
	v_mov_b32_e32 v0, v75
.LBB3_26:
	v_lshl_add_u64 v[10:11], v[0:1], 1, s[24:25]
	global_load_dwordx4 v[10:13], v[10:11], off
	v_add_u32_e32 v14, 0x880, v0
	v_mov_b32_e32 v15, v1
	v_add_u32_e32 v16, 0x1100, v0
	v_mov_b32_e32 v17, v1
	s_waitcnt vmcnt(1)
	v_lshl_add_u64 v[22:23], v[14:15], 1, s[24:25]
	v_lshl_add_u64 v[24:25], v[16:17], 1, s[24:25]
	global_load_dwordx4 v[14:17], v[22:23], off
	global_load_dwordx4 v[18:21], v[24:25], off
	v_add_u32_e32 v22, s12, v76
	ds_read_b128 v[22:25], v22
	s_add_i32 s12, s12, 64
	v_add_u32_e32 v0, 32, v0
	s_cmpk_eq_i32 s12, 0x100
	s_waitcnt vmcnt(1) lgkmcnt(0)
	v_mfma_f32_16x16x32_f16 v[114:117], v[14:17], v[22:25], v[114:117]
	v_mfma_f32_16x16x32_f16 v[110:113], v[10:13], v[22:25], v[110:113]
	s_waitcnt vmcnt(0)
	v_mfma_f32_16x16x32_f16 v[118:121], v[18:21], v[22:25], v[118:121]
	s_cbranch_scc0 .LBB3_26
	global_load_dwordx4 v[54:57], v[36:37], off
	global_load_dwordx4 v[18:21], v[38:39], off
	v_add_u32_e32 v0, v81, v68
	s_nop 3
	v_mov_b32_e32 v13, v121
	v_mov_b32_e32 v17, v117
	v_mov_b32_e32 v25, v113
	v_lshl_or_b32 v42, v0, 2, v69
	v_mov_b64_e32 v[44:45], s[30:31]
	v_mov_b32_e32 v26, v110
	v_mov_b32_e32 v27, v111
	v_mov_b32_e32 v28, v112
	v_mov_b32_e32 v29, v113
	v_mov_b32_e32 v43, v118
	v_mov_b32_e32 v46, v119
	v_mov_b32_e32 v47, v120
	v_mov_b32_e32 v48, v121
	v_mov_b32_e32 v49, v114
	v_mov_b32_e32 v50, v115
	v_mov_b32_e32 v51, v116
	v_mov_b32_e32 v52, v117
	v_mov_b32_e32 v12, v120
	v_mov_b32_e32 v11, v119
	v_mov_b32_e32 v10, v118
	v_mov_b32_e32 v16, v116
	v_mov_b32_e32 v15, v115
	v_mov_b32_e32 v14, v114
	v_mov_b32_e32 v24, v112
	v_mov_b32_e32 v23, v111
	v_mov_b32_e32 v22, v110
	v_cmp_le_i32_e64 s[12:13], v63, v82
	v_mad_i64_i32 v[44:45], s[14:15], v42, s48, v[44:45]
	s_and_saveexec_b64 s[14:15], s[12:13]
	s_cbranch_execz .LBB3_29
	v_lshlrev_b32_e32 v0, 1, v34
	v_cvt_pk_f16_f32 v29, v28, v29
	v_cvt_pk_f16_f32 v28, v26, v27
	v_lshl_add_u64 v[26:27], v[44:45], 0, v[0:1]
	global_store_dwordx2 v[26:27], v[28:29], off

.LBB3_37:
	s_endpgm
	s_nop 0
	s_nop 0
	s_nop 0
	s_nop 0
	s_nop 0
	s_nop 0
	s_nop 0
	s_nop 0
	s_nop 0
	s_nop 0
	s_nop 0
	s_nop 0
	s_nop 0
	s_nop 0
	s_nop 0
	s_nop 0
	s_nop 0
	s_nop 0
	s_nop 0
	s_nop 0
	s_nop 0
	s_nop 0
	s_nop 0
	s_nop 0
	s_nop 0
	s_nop 0
	s_nop 0
	s_nop 0
	s_nop 0
	s_nop 0
	s_nop 0
	s_nop 0
	s_nop 0
	s_nop 0
	s_nop 0
	s_nop 0
	s_nop 0
	s_nop 0
	s_nop 0
	s_endpgm

	.amdhsa_kernel _Z5k_aggILi4ELi128ELi16ELi16ELb0EEvPKiPKtPKDF16_PKfS7_S7_PvS5_S7_S7_PDF16_PfSA_
		.amdhsa_group_segment_fixed_size 39168
		.amdhsa_private_segment_fixed_size 0
		.amdhsa_kernarg_size 360
		.amdhsa_user_sgpr_count 2
		.amdhsa_user_sgpr_dispatch_ptr 0
		.amdhsa_user_sgpr_queue_ptr 0
		.amdhsa_user_sgpr_kernarg_segment_ptr 1
		.amdhsa_user_sgpr_dispatch_id 0
		.amdhsa_user_sgpr_kernarg_preload_length 0
		.amdhsa_user_sgpr_kernarg_preload_offset 0
		.amdhsa_user_sgpr_private_segment_size 0
		.amdhsa_uses_dynamic_stack 0
		.amdhsa_enable_private_segment 0
		.amdhsa_system_sgpr_workgroup_id_x 1
		.amdhsa_system_sgpr_workgroup_id_y 0
		.amdhsa_system_sgpr_workgroup_id_z 0
		.amdhsa_system_sgpr_workgroup_info 0
		.amdhsa_system_vgpr_workitem_id 0
		.amdhsa_next_free_vgpr 126
		.amdhsa_next_free_sgpr 96
		.amdhsa_accum_offset 128
		.amdhsa_reserve_vcc 1
		.amdhsa_float_round_mode_32 0
		.amdhsa_float_round_mode_16_64 0
		.amdhsa_float_denorm_mode_32 3
		.amdhsa_float_denorm_mode_16_64 3
		.amdhsa_dx10_clamp 1
		.amdhsa_ieee_mode 1
		.amdhsa_fp16_overflow 0
		.amdhsa_tg_split 0
		.amdhsa_exception_fp_ieee_invalid_op 0
		.amdhsa_exception_fp_denorm_src 0
		.amdhsa_exception_fp_ieee_div_zero 0
		.amdhsa_exception_fp_ieee_overflow 0
		.amdhsa_exception_fp_ieee_underflow 0
		.amdhsa_exception_fp_ieee_inexact 0
		.amdhsa_exception_int_div_zero 0
	.end_amdhsa_kernel

amdhsa.kernels:
  - .agpr_count:     0
    .args:
      - .actual_access:  read_only
        .address_space:  global
        .offset:         0
        .size:           8
        .value_kind:     global_buffer
      - .actual_access:  read_only
        .address_space:  global
        .offset:         8
        .size:           8
        .value_kind:     global_buffer
      - .actual_access:  write_only
        .address_space:  global
        .offset:         16
        .size:           8
        .value_kind:     global_buffer
      - .actual_access:  write_only
        .address_space:  global
        .offset:         24
        .size:           8
        .value_kind:     global_buffer
    .group_segment_fixed_size: 32320
    .kernarg_segment_align: 8
    .kernarg_segment_size: 32
    .language:       OpenCL C
    .language_version:
      - 2
      - 0
    .max_flat_workgroup_size: 1024
    .name:           _Z6k_finePKjPKtPiPt
    .private_segment_fixed_size: 0
    .sgpr_count:     71
    .sgpr_spill_count: 0
    .symbol:         _Z6k_finePKjPKtPiPt.kd
    .uniform_work_group_size: 1
    .uses_dynamic_stack: false
    .vgpr_count:     54
    .vgpr_spill_count: 0
    .wavefront_size: 64
  - .agpr_count:     0
    .args:
      - .actual_access:  read_only
        .address_space:  global
        .offset:         0
        .size:           8
        .value_kind:     global_buffer
      - .actual_access:  read_only
        .address_space:  global
        .offset:         8
        .size:           8
        .value_kind:     global_buffer
      - .actual_access:  write_only
        .address_space:  global
        .offset:         16
        .size:           8
        .value_kind:     global_buffer
      - .actual_access:  write_only
        .address_space:  global
        .offset:         24
        .size:           8
        .value_kind:     global_buffer
      - .actual_access:  read_only
        .address_space:  global
        .offset:         32
        .size:           8
        .value_kind:     global_buffer
      - .actual_access:  read_only
        .address_space:  global
        .offset:         40
        .size:           8
        .value_kind:     global_buffer
      - .actual_access:  write_only
        .address_space:  global
        .offset:         48
        .size:           8
        .value_kind:     global_buffer
      - .actual_access:  write_only
        .address_space:  global
        .offset:         56
        .size:           8
        .value_kind:     global_buffer
      - .actual_access:  read_only
        .address_space:  global
        .offset:         64
        .size:           8
        .value_kind:     global_buffer
      - .actual_access:  read_only
        .address_space:  global
        .offset:         72
        .size:           8
        .value_kind:     global_buffer
      - .actual_access:  read_only
        .address_space:  global
        .offset:         80
        .size:           8
        .value_kind:     global_buffer
      - .actual_access:  write_only
        .address_space:  global
        .offset:         88
        .size:           8
        .value_kind:     global_buffer
      - .actual_access:  write_only
        .address_space:  global
        .offset:         96
        .size:           8
        .value_kind:     global_buffer
      - .actual_access:  write_only
        .address_space:  global
        .offset:         104
        .size:           8
        .value_kind:     global_buffer
    .group_segment_fixed_size: 53248
    .kernarg_segment_align: 8
    .kernarg_segment_size: 112
    .language:       OpenCL C
    .language_version:
      - 2
      - 0
    .max_flat_workgroup_size: 256
    .name:           _Z8k_stageAPKiS0_PjPtPKfS4_PDF16_S5_S4_S4_S4_S5_PfS6_
    .private_segment_fixed_size: 0
    .sgpr_count:     75
    .sgpr_spill_count: 0
    .symbol:         _Z8k_stageAPKiS0_PjPtPKfS4_PDF16_S5_S4_S4_S4_S5_PfS6_.kd
    .uniform_work_group_size: 1
    .uses_dynamic_stack: false
    .vgpr_count:     158
    .vgpr_spill_count: 0
    .wavefront_size: 64
  - .agpr_count:     4
    .args:
      - .actual_access:  read_only
        .address_space:  global
        .offset:         0
        .size:           8
        .value_kind:     global_buffer
      - .actual_access:  read_only
        .address_space:  global
        .offset:         8
        .size:           8
        .value_kind:     global_buffer
      - .actual_access:  read_only
        .address_space:  global
        .offset:         16
        .size:           8
        .value_kind:     global_buffer
      - .actual_access:  read_only
        .address_space:  global
        .offset:         24
        .size:           8
        .value_kind:     global_buffer
      - .actual_access:  write_only
        .address_space:  global
        .offset:         32
        .size:           8
        .value_kind:     global_buffer
      - .actual_access:  write_only
        .address_space:  global
        .offset:         40
        .size:           8
        .value_kind:     global_buffer
      - .actual_access:  write_only
        .address_space:  global
        .offset:         48
        .size:           8
        .value_kind:     global_buffer
    .group_segment_fixed_size: 19584
    .kernarg_segment_align: 8
    .kernarg_segment_size: 56
    .language:       OpenCL C
    .language_version:
      - 2
      - 0
    .max_flat_workgroup_size: 256
    .name:           _Z7k_gemm2PKDF16_S0_PKfS2_PDF16_PfS4_
    .private_segment_fixed_size: 0
    .sgpr_count:     30
    .sgpr_spill_count: 0
    .symbol:         _Z7k_gemm2PKDF16_S0_PKfS2_PDF16_PfS4_.kd
    .uniform_work_group_size: 1
    .uses_dynamic_stack: false
    .vgpr_count:     84
    .vgpr_spill_count: 0
    .wavefront_size: 64
  - .agpr_count:     0
    .args:
      - .actual_access:  read_only
        .address_space:  global
        .offset:         0
        .size:           8
        .value_kind:     global_buffer
      - .actual_access:  read_only
        .address_space:  global
        .offset:         8
        .size:           8
        .value_kind:     global_buffer
      - .actual_access:  read_only
        .address_space:  global
        .offset:         16
        .size:           8
        .value_kind:     global_buffer
      - .actual_access:  read_only
        .address_space:  global
        .offset:         24
        .size:           8
        .value_kind:     global_buffer
      - .actual_access:  read_only
        .address_space:  global
        .offset:         32
        .size:           8
        .value_kind:     global_buffer
      - .actual_access:  read_only
        .address_space:  global
        .offset:         40
        .size:           8
        .value_kind:     global_buffer
      - .actual_access:  read_only
        .address_space:  global
        .offset:         48
        .size:           8
        .value_kind:     global_buffer
      - .actual_access:  read_only
        .address_space:  global
        .offset:         56
        .size:           8
        .value_kind:     global_buffer
      - .actual_access:  read_only
        .address_space:  global
        .offset:         64
        .size:           8
        .value_kind:     global_buffer
      - .actual_access:  read_only
        .address_space:  global
        .offset:         72
        .size:           8
        .value_kind:     global_buffer
      - .actual_access:  write_only
        .address_space:  global
        .offset:         80
        .size:           8
        .value_kind:     global_buffer
      - .actual_access:  write_only
        .address_space:  global
        .offset:         88
        .size:           8
        .value_kind:     global_buffer
      - .actual_access:  write_only
        .address_space:  global
        .offset:         96
        .size:           8
        .value_kind:     global_buffer
      - .offset:         104
        .size:           4
        .value_kind:     hidden_block_count_x
      - .offset:         108
        .size:           4
        .value_kind:     hidden_block_count_y
      - .offset:         112
        .size:           4
        .value_kind:     hidden_block_count_z
      - .offset:         116
        .size:           2
        .value_kind:     hidden_group_size_x
      - .offset:         118
        .size:           2
        .value_kind:     hidden_group_size_y
      - .offset:         120
        .size:           2
        .value_kind:     hidden_group_size_z
      - .offset:         122
        .size:           2
        .value_kind:     hidden_remainder_x
      - .offset:         124
        .size:           2
        .value_kind:     hidden_remainder_y
      - .offset:         126
        .size:           2
        .value_kind:     hidden_remainder_z
      - .offset:         144
        .size:           8
        .value_kind:     hidden_global_offset_x
      - .offset:         152
        .size:           8
        .value_kind:     hidden_global_offset_y
      - .offset:         160
        .size:           8
        .value_kind:     hidden_global_offset_z
      - .offset:         168
        .size:           2
        .value_kind:     hidden_grid_dims
    .group_segment_fixed_size: 39168
    .kernarg_segment_align: 8
    .kernarg_segment_size: 360
    .language:       OpenCL C
    .language_version:
      - 2
      - 0
    .max_flat_workgroup_size: 256
    .name:           _Z5k_aggILi4ELi128ELi16ELi16ELb0EEvPKiPKtPKDF16_PKfS7_S7_PvS5_S7_S7_PDF16_PfSA_
    .private_segment_fixed_size: 0
    .sgpr_count:     55
    .sgpr_spill_count: 0
    .symbol:         _Z5k_aggILi4ELi128ELi16ELi16ELb0EEvPKiPKtPKDF16_PKfS7_S7_PvS5_S7_S7_PDF16_PfSA_.kd
    .uniform_work_group_size: 1
    .uses_dynamic_stack: false
    .vgpr_count:     126
    .vgpr_spill_count: 0
    .wavefront_size: 64
  - .agpr_count:     0
    .args:
      - .actual_access:  read_only
        .address_space:  global
        .offset:         0
        .size:           8
        .value_kind:     global_buffer
      - .actual_access:  read_only
        .address_space:  global
        .offset:         8
        .size:           8
        .value_kind:     global_buffer
      - .actual_access:  read_only
        .address_space:  global
        .offset:         16
        .size:           8
        .value_kind:     global_buffer
      - .actual_access:  read_only
        .address_space:  global
        .offset:         24
        .size:           8
        .value_kind:     global_buffer
      - .actual_access:  read_only
        .address_space:  global
        .offset:         32
        .size:           8
        .value_kind:     global_buffer
      - .actual_access:  read_only
        .address_space:  global
        .offset:         40
        .size:           8
        .value_kind:     global_buffer
      - .actual_access:  write_only
        .address_space:  global
        .offset:         48
        .size:           8
        .value_kind:     global_buffer
      - .actual_access:  read_only
        .address_space:  global
        .offset:         56
        .size:           8
        .value_kind:     global_buffer
      - .actual_access:  read_only
        .address_space:  global
        .offset:         64
        .size:           8
        .value_kind:     global_buffer
      - .actual_access:  read_only
        .address_space:  global
        .offset:         72
        .size:           8
        .value_kind:     global_buffer
      - .actual_access:  read_only
        .address_space:  global
        .offset:         80
        .size:           8
        .value_kind:     global_buffer
      - .actual_access:  read_only
        .address_space:  global
        .offset:         88
        .size:           8
        .value_kind:     global_buffer
      - .actual_access:  read_only
        .address_space:  global
        .offset:         96
        .size:           8
        .value_kind:     global_buffer
      - .offset:         104
        .size:           4
        .value_kind:     hidden_block_count_x
      - .offset:         108
        .size:           4
        .value_kind:     hidden_block_count_y
      - .offset:         112
        .size:           4
        .value_kind:     hidden_block_count_z
      - .offset:         116
        .size:           2
        .value_kind:     hidden_group_size_x
      - .offset:         118
        .size:           2
        .value_kind:     hidden_group_size_y
      - .offset:         120
        .size:           2
        .value_kind:     hidden_group_size_z
      - .offset:         122
        .size:           2
        .value_kind:     hidden_remainder_x
      - .offset:         124
        .size:           2
        .value_kind:     hidden_remainder_y
      - .offset:         126
        .size:           2
        .value_kind:     hidden_remainder_z
      - .offset:         144
        .size:           8
        .value_kind:     hidden_global_offset_x
      - .offset:         152
        .size:           8
        .value_kind:     hidden_global_offset_y
      - .offset:         160
        .size:           8
        .value_kind:     hidden_global_offset_z
      - .offset:         168
        .size:           2
        .value_kind:     hidden_grid_dims
    .group_segment_fixed_size: 8704
    .kernarg_segment_align: 8
    .kernarg_segment_size: 360
    .language:       OpenCL C
    .language_version:
      - 2
      - 0
    .max_flat_workgroup_size: 256
    .name:           _Z5k_aggILi1ELi40ELi5ELi5ELb1EEvPKiPKtPKDF16_PKfS7_S7_PvS5_S7_S7_PDF16_PfSA_
    .private_segment_fixed_size: 0
    .sgpr_count:     31
    .sgpr_spill_count: 0
    .symbol:         _Z5k_aggILi1ELi40ELi5ELi5ELb1EEvPKiPKtPKDF16_PKfS7_S7_PvS5_S7_S7_PDF16_PfSA_.kd
    .uniform_work_group_size: 1
    .uses_dynamic_stack: false
    .vgpr_count:     75
    .vgpr_spill_count: 0
    .wavefront_size: 64
